# v35
# speedup vs baseline: 1.0161x; 1.0027x over previous
.LBB0_2:
	v_lshl_add_u64 v[2:3], v[2:3], 0, s[10:11]
	v_lshl_add_u64 v[8:9], v[6:7], 0, s[14:15]
	v_cmp_lt_u64_e32 vcc, s[12:13], v[2:3]
	v_and_b32_e32 v1, 0x1ff, v2
	v_lshlrev_b32_e32 v4, 5, v1
	v_cndmask_b32_e32 v17, v7, v9, vcc
	v_cndmask_b32_e32 v16, v6, v8, vcc
	v_lshlrev_b64 v[8:9], 14, v[16:17]
	v_lshl_add_u64 v[8:9], s[6:7], 0, v[8:9]
	v_lshl_add_u64 v[18:19], v[8:9], 0, v[4:5]
	global_load_dwordx4 v[8:11], v[18:19], off nt
	global_load_dwordx4 v[12:15], v[18:19], off offset:16 nt
	v_lshlrev_b32_e32 v4, 1, v16
	v_and_b32_e32 v16, 0x7f, v16
	v_and_b32_e32 v4, 0x7f00, v4
	v_or3_b32 v4, v16, v4, s3
	v_lshlrev_b32_e32 v4, 13, v4
	v_lshl_add_u64 v[16:17], s[4:5], 0, v[4:5]
	v_lshlrev_b32_e32 v4, 4, v1
	v_lshl_add_u64 v[16:17], v[16:17], 0, v[4:5]
	v_cmp_lt_u64_e32 vcc, s[18:19], v[2:3]
	v_lshl_add_u64 v[6:7], v[6:7], 0, s[16:17]
	s_or_b64 s[8:9], vcc, s[8:9]
	s_waitcnt vmcnt(1)
	v_cvt_pkrtz_f16_f32 v1, v8, v9
	v_cvt_pkrtz_f16_f32 v4, v10, v11
	s_waitcnt vmcnt(0)
	v_cvt_pkrtz_f16_f32 v8, v12, v13
	v_cvt_pkrtz_f16_f32 v9, v14, v15
	v_add_u32_e32 v1, 0x20002, v1
	v_add_u32_e32 v4, 0x20002, v4
	v_add_u32_e32 v10, 0x20002, v8
	v_add_u32_e32 v11, 0x20002, v9
	v_and_b32_e32 v8, 0xfffcfffc, v1
	v_and_b32_e32 v9, 0xfffcfffc, v4
	v_and_b32_e32 v10, 0xfffcfffc, v10
	v_and_b32_e32 v11, 0xfffcfffc, v11
	global_store_dwordx4 v[16:17], v[8:11], off sc1
	s_andn2_b64 exec, exec, s[8:9]
	s_cbranch_execnz .LBB0_2
	s_or_b64 exec, exec, s[8:9]
	s_mov_b64 s[4:5], 0

.LBB0_6:
	v_lshl_add_u64 v[46:47], v[2:3], 0, s[0:1]
	v_lshl_add_u64 v[50:51], v[4:5], 0, s[0:1]
	global_load_dwordx4 v[10:13], v[46:47], off nt
	global_load_dwordx4 v[14:17], v[50:51], off
	global_load_dwordx4 v[18:21], v[46:47], off offset:16 nt
	global_load_dwordx4 v[22:25], v[46:47], off offset:128 nt
	global_load_dwordx4 v[26:29], v[46:47], off offset:144 nt
	global_load_dwordx4 v[30:33], v[46:47], off offset:256 nt
	global_load_dwordx4 v[34:37], v[46:47], off offset:272 nt
	s_add_u32 s0, s0, 0x200
	s_addc_u32 s1, s1, 0
	s_cmpk_eq_i32 s0, 0x1000
	s_waitcnt vmcnt(5)
	v_mfma_f32_16x16x4_f32 a[0:3], v10, v14, a[0:3]
	v_cvt_pkrtz_f16_f32 v10, v10, v11
	v_add_u32_e32 v10, 0x20002, v10
	v_and_b32_e32 v10, 0xfffcfffc, v10
	v_mfma_f32_16x16x4_f32 a[0:3], v11, v15, a[0:3]
	v_cvt_pkrtz_f16_f32 v11, v12, v13
	v_add_u32_e32 v11, 0x20002, v11
	v_and_b32_e32 v11, 0xfffcfffc, v11
	v_mfma_f32_16x16x4_f32 a[0:3], v12, v16, a[0:3]
	s_waitcnt vmcnt(4)
	v_cvt_pkrtz_f16_f32 v12, v18, v19
	v_add_u32_e32 v12, 0x20002, v12
	v_and_b32_e32 v12, 0xfffcfffc, v12
	v_mfma_f32_16x16x4_f32 a[0:3], v13, v17, a[0:3]
	global_load_dwordx4 v[14:17], v[50:51], off offset:16
	v_cvt_pkrtz_f16_f32 v13, v20, v21
	v_add_u32_e32 v13, 0x20002, v13
	v_and_b32_e32 v13, 0xfffcfffc, v13
	s_waitcnt vmcnt(0)
	v_mfma_f32_16x16x4_f32 a[0:3], v18, v14, a[0:3]
	v_cvt_pkrtz_f16_f32 v18, v22, v23
	v_add_u32_e32 v18, 0x20002, v18
	v_and_b32_e32 v18, 0xfffcfffc, v18
	v_mfma_f32_16x16x4_f32 a[0:3], v19, v15, a[0:3]
	v_cvt_pkrtz_f16_f32 v19, v24, v25
	v_add_u32_e32 v19, 0x20002, v19
	v_and_b32_e32 v19, 0xfffcfffc, v19
	v_mfma_f32_16x16x4_f32 a[0:3], v20, v16, a[0:3]
	v_cvt_pkrtz_f16_f32 v20, v26, v27
	v_add_u32_e32 v20, 0x20002, v20
	v_and_b32_e32 v20, 0xfffcfffc, v20
	v_mfma_f32_16x16x4_f32 a[0:3], v21, v17, a[0:3]
	global_load_dwordx4 v[14:17], v[50:51], off offset:128
	v_cvt_pkrtz_f16_f32 v21, v28, v29
	v_add_u32_e32 v21, 0x20002, v21
	v_and_b32_e32 v21, 0xfffcfffc, v21
	s_waitcnt vmcnt(0)
	v_mfma_f32_16x16x4_f32 a[0:3], v22, v14, a[0:3]
	v_cvt_pkrtz_f16_f32 v22, v30, v31
	v_add_u32_e32 v22, 0x20002, v22
	v_and_b32_e32 v22, 0xfffcfffc, v22
	v_mfma_f32_16x16x4_f32 a[0:3], v23, v15, a[0:3]
	v_cvt_pkrtz_f16_f32 v23, v32, v33
	v_mfma_f32_16x16x4_f32 a[0:3], v24, v16, a[0:3]
	v_cvt_pkrtz_f16_f32 v24, v34, v35
	v_add_u32_e32 v24, 0x20002, v24
	v_and_b32_e32 v24, 0xfffcfffc, v24
	v_mfma_f32_16x16x4_f32 a[0:3], v25, v17, a[0:3]
	global_load_dwordx4 v[14:17], v[50:51], off offset:144
	v_cvt_pkrtz_f16_f32 v25, v36, v37
	v_add_u32_e32 v25, 0x20002, v25
	v_and_b32_e32 v25, 0xfffcfffc, v25
	s_waitcnt vmcnt(0)
	v_mfma_f32_16x16x4_f32 a[0:3], v26, v14, a[0:3]
	v_mfma_f32_16x16x4_f32 a[0:3], v27, v15, a[0:3]
	v_mfma_f32_16x16x4_f32 a[0:3], v28, v16, a[0:3]
	v_mfma_f32_16x16x4_f32 a[0:3], v29, v17, a[0:3]
	global_load_dwordx4 v[14:17], v[50:51], off offset:256
	s_waitcnt vmcnt(0)
	v_mfma_f32_16x16x4_f32 a[0:3], v30, v14, a[0:3]
	v_mfma_f32_16x16x4_f32 a[0:3], v31, v15, a[0:3]
	v_mfma_f32_16x16x4_f32 a[0:3], v32, v16, a[0:3]
	v_mfma_f32_16x16x4_f32 a[0:3], v33, v17, a[0:3]
	global_load_dwordx4 v[14:17], v[50:51], off offset:272
	global_load_dwordx4 v[38:41], v[46:47], off offset:384 nt
	global_load_dwordx4 v[42:45], v[46:47], off offset:400 nt
	s_waitcnt vmcnt(1)
	v_cvt_pkrtz_f16_f32 v26, v38, v39
	global_load_dwordx4 v[46:49], v[50:51], off offset:384
	v_mfma_f32_16x16x4_f32 a[0:3], v34, v14, a[0:3]
	v_cvt_pkrtz_f16_f32 v27, v40, v41
	s_waitcnt vmcnt(1)
	v_cvt_pkrtz_f16_f32 v28, v42, v43
	v_cvt_pkrtz_f16_f32 v29, v44, v45
	v_add_u32_e32 v26, 0x20002, v26
	v_add_u32_e32 v27, 0x20002, v27
	v_add_u32_e32 v28, 0x20002, v28
	v_add_u32_e32 v29, 0x20002, v29
	v_mfma_f32_16x16x4_f32 a[0:3], v35, v15, a[0:3]
	v_mfma_f32_16x16x4_f32 a[0:3], v36, v16, a[0:3]
	v_mfma_f32_16x16x4_f32 a[0:3], v37, v17, a[0:3]
	global_load_dwordx4 v[14:17], v[50:51], off offset:400
	s_waitcnt vmcnt(1)
	v_mfma_f32_16x16x4_f32 a[0:3], v38, v46, a[0:3]
	v_mfma_f32_16x16x4_f32 a[0:3], v39, v47, a[0:3]
	v_mfma_f32_16x16x4_f32 a[0:3], v40, v48, a[0:3]
	v_mfma_f32_16x16x4_f32 a[0:3], v41, v49, a[0:3]
	s_waitcnt vmcnt(0)
	v_mfma_f32_16x16x4_f32 a[0:3], v42, v14, a[0:3]
	v_add_u32_e32 v14, 0x20002, v23
	v_and_b32_e32 v23, 0xfffcfffc, v14
	v_and_b32_e32 v14, 0xfffcfffc, v26
	v_mfma_f32_16x16x4_f32 a[0:3], v43, v15, a[0:3]
	v_and_b32_e32 v15, 0xfffcfffc, v27
	v_mfma_f32_16x16x4_f32 a[0:3], v44, v16, a[0:3]
	v_and_b32_e32 v16, 0xfffcfffc, v28
	v_mfma_f32_16x16x4_f32 a[0:3], v45, v17, a[0:3]
	v_and_b32_e32 v17, 0xfffcfffc, v29
	global_store_dwordx4 v[6:7], v[10:13], off offset:-128 sc1
	global_store_dwordx4 v[6:7], v[18:21], off offset:-64 sc1
	global_store_dwordx4 v[6:7], v[22:25], off sc1
	global_store_dwordx4 v[6:7], v[14:17], off offset:64 sc1
	v_lshl_add_u64 v[6:7], v[6:7], 0, s[2:3]
	s_cbranch_scc0 .LBB0_6
	v_mul_u32_u24_e32 v2, 0x440, v8
	v_mul_u32_u24_e32 v3, 0x110, v9
	v_lshlrev_b32_e32 v1, 2, v1
	v_add3_u32 v1, v2, v3, v1
	v_cmp_gt_u32_e32 vcc, 16, v0
	ds_write_b32 v1, a0
	ds_write_b32 v1, a1 offset:68
	ds_write_b32 v1, a2 offset:136
	ds_write_b32 v1, a3 offset:204
	s_waitcnt lgkmcnt(0)
	s_barrier
	s_and_saveexec_b64 s[0:1], vcc
	s_cbranch_execz .LBB0_13
	s_movk_i32 s0, 0x44
	v_mov_b32_e32 v2, 0x440
	v_mov_b32_e32 v3, 0x880
	v_mov_b32_e32 v4, 0xcc0
	v_mul_u32_u24_e32 v1, 0x44, v0
	v_mad_u32_u24 v2, v0, s0, v2
	v_mad_u32_u24 v3, v0, s0, v3
	v_mad_u32_u24 v4, v0, s0, v4
	ds_read2_b32 v[10:11], v1 offset1:1
	ds_read2_b32 v[12:13], v2 offset1:1
	ds_read2_b32 v[2:3], v3 offset1:1
	ds_read2_b32 v[4:5], v4 offset1:1
	ds_read2_b32 v[16:17], v1 offset0:2 offset1:3
	ds_read2_b32 v[18:19], v1 offset0:4 offset1:5
	ds_read2_b32 v[20:21], v1 offset0:6 offset1:7
	s_waitcnt lgkmcnt(4)
	v_mov_b32_e32 v7, v2
	s_waitcnt lgkmcnt(3)
	v_mov_b32_e32 v9, v4
	v_mov_b32_e32 v2, v11
	v_mov_b32_e32 v4, v13
	v_pk_add_f32 v[2:3], v[2:3], v[4:5]
	v_mov_b32_e32 v6, v10
	v_mov_b32_e32 v1, 0x448
	v_mov_b32_e32 v8, v12
	v_add_f32_e32 v14, v2, v3
	v_mov_b32_e32 v2, 0x888
	v_mad_u32_u24 v1, v0, s0, v1
	v_pk_add_f32 v[6:7], v[6:7], v[8:9]
	v_mad_u32_u24 v2, v0, s0, v2
	ds_read2_b32 v[22:23], v1 offset1:1
	ds_read2_b32 v[2:3], v2 offset1:1
	v_add_f32_e32 v1, v6, v7
	v_mov_b32_e32 v6, 0x450
	v_mov_b32_e32 v4, 0xcc8
	v_mad_u32_u24 v8, v0, s0, v6
	v_mov_b32_e32 v6, 0x890
	v_mad_u32_u24 v5, v0, s0, v4
	v_mad_u32_u24 v9, v0, s0, v6
	ds_read2_b32 v[6:7], v5 offset1:1
	ds_read2_b32 v[24:25], v8 offset1:1
	ds_read2_b32 v[8:9], v9 offset1:1
	s_waitcnt lgkmcnt(3)
	v_mov_b32_e32 v5, v2
	v_mov_b32_e32 v2, v17
	s_waitcnt lgkmcnt(2)
	v_mov_b32_e32 v11, v6
	v_mov_b32_e32 v6, v23
	v_pk_add_f32 v[2:3], v[2:3], v[6:7]
	v_mov_b32_e32 v4, v16
	v_add_f32_e32 v16, v2, v3
	v_mov_b32_e32 v2, 0xcd0
	v_mov_b32_e32 v10, v22
	v_mad_u32_u24 v2, v0, s0, v2
	v_pk_add_f32 v[4:5], v[4:5], v[10:11]
	ds_read2_b32 v[2:3], v2 offset1:1
	v_mov_b32_e32 v7, 0x458
	v_mov_b32_e32 v10, 0xcd8
	v_add_f32_e32 v15, v4, v5
	s_waitcnt lgkmcnt(1)
	v_mov_b32_e32 v5, v8
	v_mad_u32_u24 v7, v0, s0, v7
	v_mov_b32_e32 v8, 0x898
	v_mad_u32_u24 v12, v0, s0, v10
	v_mad_u32_u24 v8, v0, s0, v8
	ds_read2_b32 v[22:23], v7 offset1:1
	ds_read2_b32 v[10:11], v8 offset1:1
	ds_read2_b32 v[12:13], v12 offset1:1
	v_mov_b32_e32 v4, v18
	v_mov_b32_e32 v6, v24
	s_waitcnt lgkmcnt(3)
	v_mov_b32_e32 v7, v2
	v_mov_b32_e32 v8, v19
	v_mov_b32_e32 v2, v25
	v_pk_add_f32 v[4:5], v[4:5], v[6:7]
	v_pk_add_f32 v[2:3], v[8:9], v[2:3]
	v_add_f32_e32 v6, v4, v5
	v_add_f32_e32 v7, v2, v3
	v_mov_b32_e32 v2, v20
	s_waitcnt lgkmcnt(1)
	v_mov_b32_e32 v3, v10
	v_mov_b32_e32 v4, v22
	s_waitcnt lgkmcnt(0)
	v_mov_b32_e32 v5, v12
	v_pk_add_f32 v[2:3], v[2:3], v[4:5]
	v_mov_b32_e32 v10, v21
	v_mov_b32_e32 v12, v23
	v_add_f32_e32 v4, v2, v3
	v_pk_add_f32 v[2:3], v[10:11], v[12:13]
	s_mov_b32 s0, 0x3fb8aa3b
	v_add_f32_e32 v2, v2, v3
	v_max_f32_e32 v3, v1, v14
	v_max3_f32 v3, v3, v15, v16
	v_max3_f32 v3, v3, v6, v7
	v_max3_f32 v3, v3, v4, v2
	v_sub_f32_e32 v1, v1, v3
	v_mul_f32_e32 v5, 0x3fb8aa3b, v1
	v_fma_f32 v8, v1, s0, -v5
	v_rndne_f32_e32 v9, v5
	v_fmac_f32_e32 v8, 0x32a5705f, v1
	v_sub_f32_e32 v5, v5, v9
	v_add_f32_e32 v5, v5, v8
	v_exp_f32_e32 v5, v5
	v_cvt_i32_f32_e32 v8, v9
	s_mov_b32 s1, 0xc2ce8ed0
	v_cmp_ngt_f32_e32 vcc, s1, v1
	s_mov_b32 s2, 0x42b17218
	v_ldexp_f32 v5, v5, v8
	v_sub_f32_e32 v8, v14, v3
	v_mul_f32_e32 v9, 0x3fb8aa3b, v8
	v_fma_f32 v10, v8, s0, -v9
	v_rndne_f32_e32 v11, v9
	v_fmac_f32_e32 v10, 0x32a5705f, v8
	v_sub_f32_e32 v9, v9, v11
	v_add_f32_e32 v9, v9, v10
	v_exp_f32_e32 v9, v9
	v_cvt_i32_f32_e32 v10, v11
	v_cndmask_b32_e32 v5, 0, v5, vcc
	v_mov_b32_e32 v11, 0x7f800000
	v_cmp_nlt_f32_e32 vcc, s2, v1
	v_sub_f32_e32 v6, v6, v3
	v_sub_f32_e32 v7, v7, v3
	v_cndmask_b32_e32 v1, v11, v5, vcc
	v_ldexp_f32 v5, v9, v10
	v_sub_f32_e32 v9, v15, v3
	v_mul_f32_e32 v10, 0x3fb8aa3b, v9
	v_fma_f32 v12, v9, s0, -v10
	v_rndne_f32_e32 v13, v10
	v_fmac_f32_e32 v12, 0x32a5705f, v9
	v_sub_f32_e32 v10, v10, v13
	v_add_f32_e32 v10, v10, v12
	v_exp_f32_e32 v10, v10
	v_cvt_i32_f32_e32 v12, v13
	v_cmp_ngt_f32_e32 vcc, s1, v8
	v_sub_f32_e32 v4, v4, v3
	v_sub_f32_e32 v2, v2, v3
	v_ldexp_f32 v10, v10, v12
	v_sub_f32_e32 v12, v16, v3
	v_mul_f32_e32 v13, 0x3fb8aa3b, v12
	v_fma_f32 v14, v12, s0, -v13
	v_rndne_f32_e32 v15, v13
	v_fmac_f32_e32 v14, 0x32a5705f, v12
	v_sub_f32_e32 v13, v13, v15
	v_add_f32_e32 v13, v13, v14
	v_exp_f32_e32 v13, v13
	v_cvt_i32_f32_e32 v14, v15
	v_cndmask_b32_e32 v5, 0, v5, vcc
	v_cmp_nlt_f32_e32 vcc, s2, v8
	v_mul_f32_e32 v3, 0x3fb8aa3b, v2
	s_nop 0
	v_cndmask_b32_e32 v5, v11, v5, vcc
	v_cmp_ngt_f32_e32 vcc, s1, v9
	v_add_f32_e32 v8, v1, v5
	s_nop 0
	v_cndmask_b32_e32 v10, 0, v10, vcc
	v_cmp_nlt_f32_e32 vcc, s2, v9
	s_nop 1
	v_cndmask_b32_e32 v9, v11, v10, vcc
	v_ldexp_f32 v10, v13, v14
	v_mul_f32_e32 v13, 0x3fb8aa3b, v6
	v_fma_f32 v14, v6, s0, -v13
	v_rndne_f32_e32 v15, v13
	v_fmac_f32_e32 v14, 0x32a5705f, v6
	v_sub_f32_e32 v13, v13, v15
	v_add_f32_e32 v13, v13, v14
	v_exp_f32_e32 v13, v13
	v_cvt_i32_f32_e32 v14, v15
	v_cmp_ngt_f32_e32 vcc, s1, v12
	v_add_f32_e32 v8, v9, v8
	s_nop 0
	v_cndmask_b32_e32 v10, 0, v10, vcc
	v_cmp_nlt_f32_e32 vcc, s2, v12
	v_ldexp_f32 v12, v13, v14
	v_mul_f32_e32 v13, 0x3fb8aa3b, v7
	v_fma_f32 v14, v7, s0, -v13
	v_rndne_f32_e32 v15, v13
	v_fmac_f32_e32 v14, 0x32a5705f, v7
	v_sub_f32_e32 v13, v13, v15
	v_add_f32_e32 v13, v13, v14
	v_exp_f32_e32 v13, v13
	v_cvt_i32_f32_e32 v14, v15
	v_cndmask_b32_e32 v10, v11, v10, vcc
	v_cmp_ngt_f32_e32 vcc, s1, v6
	v_add_f32_e32 v8, v10, v8
	s_nop 0
	v_cndmask_b32_e32 v12, 0, v12, vcc
	v_cmp_nlt_f32_e32 vcc, s2, v6
	s_nop 1
	v_cndmask_b32_e32 v6, v11, v12, vcc
	v_ldexp_f32 v12, v13, v14
	v_mul_f32_e32 v13, 0x3fb8aa3b, v4
	v_fma_f32 v14, v4, s0, -v13
	v_rndne_f32_e32 v15, v13
	v_fmac_f32_e32 v14, 0x32a5705f, v4
	v_sub_f32_e32 v13, v13, v15
	v_add_f32_e32 v13, v13, v14
	v_exp_f32_e32 v13, v13
	v_cvt_i32_f32_e32 v14, v15
	v_cmp_ngt_f32_e32 vcc, s1, v7
	v_add_f32_e32 v8, v6, v8
	s_nop 0
	v_cndmask_b32_e32 v12, 0, v12, vcc
	v_cmp_nlt_f32_e32 vcc, s2, v7
	s_nop 1
	v_cndmask_b32_e32 v7, v11, v12, vcc
	v_ldexp_f32 v12, v13, v14
	v_fma_f32 v13, v2, s0, -v3
	v_rndne_f32_e32 v14, v3
	v_fmac_f32_e32 v13, 0x32a5705f, v2
	v_sub_f32_e32 v3, v3, v14
	v_add_f32_e32 v3, v3, v13
	v_exp_f32_e32 v3, v3
	v_cvt_i32_f32_e32 v13, v14
	v_cmp_ngt_f32_e32 vcc, s1, v4
	v_add_f32_e32 v8, v7, v8
	v_ldexp_f32 v3, v3, v13
	v_cndmask_b32_e32 v12, 0, v12, vcc
	v_cmp_nlt_f32_e32 vcc, s2, v4
	s_nop 1
	v_cndmask_b32_e32 v4, v11, v12, vcc
	v_cmp_ngt_f32_e32 vcc, s1, v2
	v_add_f32_e32 v8, v4, v8
	s_nop 0
	v_cndmask_b32_e32 v3, 0, v3, vcc
	v_cmp_nlt_f32_e32 vcc, s2, v2
	s_nop 1
	v_cndmask_b32_e32 v2, v11, v3, vcc
	v_add_f32_e32 v3, v2, v8
	v_div_scale_f32 v8, s[0:1], v3, v3, v1
	v_rcp_f32_e32 v11, v8
	s_nop 0
	v_fma_f32 v12, -v8, v11, 1.0
	v_fmac_f32_e32 v11, v12, v11
	v_div_scale_f32 v12, vcc, v1, v3, v1
	v_mul_f32_e32 v13, v12, v11
	v_fma_f32 v14, -v8, v13, v12
	v_fmac_f32_e32 v13, v14, v11
	v_fma_f32 v8, -v8, v13, v12
	v_div_scale_f32 v12, s[0:1], v3, v3, v5
	v_rcp_f32_e32 v14, v12
	v_div_fmas_f32 v8, v8, v11, v13
	v_div_fixup_f32 v8, v8, v3, v1
	v_cmp_lt_f32_e64 s[6:7], -1.0, v8
	v_fma_f32 v1, -v12, v14, 1.0
	v_fmac_f32_e32 v14, v1, v14
	v_div_scale_f32 v1, vcc, v5, v3, v5
	v_mul_f32_e32 v11, v1, v14
	v_fma_f32 v13, -v12, v11, v1
	v_fmac_f32_e32 v11, v13, v14
	v_fma_f32 v1, -v12, v11, v1
	v_div_scale_f32 v12, s[0:1], v3, v3, v9
	v_rcp_f32_e32 v13, v12
	v_div_fmas_f32 v1, v1, v14, v11
	v_div_fixup_f32 v5, v1, v3, v5
	v_fma_f32 v1, -v12, v13, 1.0
	v_fmac_f32_e32 v13, v1, v13
	v_div_scale_f32 v1, vcc, v9, v3, v9
	v_mul_f32_e32 v11, v1, v13
	v_fma_f32 v14, -v12, v11, v1
	v_fmac_f32_e32 v11, v14, v13
	v_fma_f32 v1, -v12, v11, v1
	v_div_scale_f32 v12, s[0:1], v3, v3, v10
	v_rcp_f32_e32 v14, v12
	v_div_fmas_f32 v1, v1, v13, v11
	v_div_fixup_f32 v9, v1, v3, v9
	v_fma_f32 v1, -v12, v14, 1.0
	v_fmac_f32_e32 v14, v1, v14
	v_div_scale_f32 v1, vcc, v10, v3, v10
	v_mul_f32_e32 v11, v1, v14
	v_fma_f32 v13, -v12, v11, v1
	v_fmac_f32_e32 v11, v13, v14
	v_fma_f32 v1, -v12, v11, v1
	v_div_scale_f32 v12, s[0:1], v3, v3, v6
	v_rcp_f32_e32 v13, v12
	v_div_fmas_f32 v1, v1, v14, v11
	v_div_fixup_f32 v10, v1, v3, v10
	v_fma_f32 v1, -v12, v13, 1.0
	v_fmac_f32_e32 v13, v1, v13
	v_div_scale_f32 v1, vcc, v6, v3, v6
	v_mul_f32_e32 v11, v1, v13
	v_fma_f32 v14, -v12, v11, v1
	v_fmac_f32_e32 v11, v14, v13
	v_fma_f32 v1, -v12, v11, v1
	v_div_scale_f32 v12, s[0:1], v3, v3, v7
	v_rcp_f32_e32 v14, v12
	v_div_fmas_f32 v1, v1, v13, v11
	v_div_fixup_f32 v6, v1, v3, v6
	v_fma_f32 v1, -v12, v14, 1.0
	v_fmac_f32_e32 v14, v1, v14
	v_div_scale_f32 v1, vcc, v7, v3, v7
	v_mul_f32_e32 v11, v1, v14
	v_fma_f32 v13, -v12, v11, v1
	v_fmac_f32_e32 v11, v13, v14
	v_fma_f32 v1, -v12, v11, v1
	v_div_scale_f32 v12, s[0:1], v3, v3, v4
	v_rcp_f32_e32 v13, v12
	v_div_fmas_f32 v1, v1, v14, v11
	v_div_fixup_f32 v7, v1, v3, v7
	v_fma_f32 v1, -v12, v13, 1.0
	v_fmac_f32_e32 v13, v1, v13
	v_div_scale_f32 v1, vcc, v4, v3, v4
	v_mul_f32_e32 v11, v1, v13
	v_fma_f32 v14, -v12, v11, v1
	v_fmac_f32_e32 v11, v14, v13
	v_fma_f32 v1, -v12, v11, v1
	v_div_scale_f32 v12, s[0:1], v3, v3, v2
	v_rcp_f32_e32 v14, v12
	v_div_fmas_f32 v1, v1, v13, v11
	v_div_fixup_f32 v4, v1, v3, v4
	v_fma_f32 v1, -v12, v14, 1.0
	v_fmac_f32_e32 v14, v1, v14
	v_div_scale_f32 v1, vcc, v2, v3, v2
	v_mul_f32_e32 v11, v1, v14
	v_fma_f32 v13, -v12, v11, v1
	v_fmac_f32_e32 v11, v13, v14
	v_fma_f32 v1, -v12, v11, v1
	v_div_fmas_f32 v1, v1, v14, v11
	v_cmp_gt_f32_e32 vcc, v5, v8
	v_div_fixup_f32 v1, v1, v3, v2
	s_nop 0
	v_cndmask_b32_e32 v3, v8, v5, vcc
	v_cndmask_b32_e64 v2, 0, 1, vcc
	v_cmp_gt_f32_e32 vcc, v9, v3
	s_nop 1
	v_cndmask_b32_e32 v3, v3, v9, vcc
	v_cndmask_b32_e64 v2, v2, 2, vcc
	v_cmp_gt_f32_e32 vcc, v10, v3
	s_nop 1
	v_cndmask_b32_e32 v3, v3, v10, vcc
	v_cndmask_b32_e64 v2, v2, 3, vcc
	v_cmp_gt_f32_e32 vcc, v6, v3
	s_nop 1
	v_cndmask_b32_e32 v3, v3, v6, vcc
	v_cndmask_b32_e64 v2, v2, 4, vcc
	v_cmp_gt_f32_e32 vcc, v7, v3
	s_nop 1
	v_cndmask_b32_e32 v3, v3, v7, vcc
	v_cndmask_b32_e64 v2, v2, 5, vcc
	v_cmp_ngt_f32_e32 vcc, v4, v3
	s_nop 1
	v_cndmask_b32_e32 v3, v4, v3, vcc
	v_cndmask_b32_e32 v2, 6, v2, vcc
	v_cmp_gt_f32_e64 s[2:3], v1, v3
	v_cmp_ngt_f32_e64 s[0:1], v1, v3
	s_nop 0
	v_cndmask_b32_e64 v2, v2, 7, s[2:3]
	v_cmp_ne_u32_e64 s[4:5], 0, v2
	s_and_b64 s[4:5], s[6:7], s[4:5]
	s_or_b64 s[2:3], vcc, s[2:3]
	v_cndmask_b32_e64 v8, -1.0, v8, s[4:5]
	v_cmp_ne_u32_e64 s[4:5], 1, v2
	v_cmp_gt_f32_e64 s[6:7], v5, v8
	s_and_b64 s[4:5], s[4:5], s[6:7]
	v_cndmask_b32_e64 v5, v8, v5, s[4:5]
	v_cmp_ne_u32_e64 s[4:5], 2, v2
	v_cmp_gt_f32_e64 s[6:7], v9, v5
	s_and_b64 s[4:5], s[4:5], s[6:7]
	v_cndmask_b32_e64 v5, v5, v9, s[4:5]
	v_cmp_ne_u32_e64 s[4:5], 3, v2
	v_cmp_gt_f32_e64 s[6:7], v10, v5
	s_and_b64 s[4:5], s[4:5], s[6:7]
	v_cndmask_b32_e64 v5, v5, v10, s[4:5]
	v_cmp_ne_u32_e64 s[4:5], 4, v2
	v_cmp_gt_f32_e64 s[6:7], v6, v5
	s_and_b64 s[4:5], s[4:5], s[6:7]
	v_cndmask_b32_e64 v5, v5, v6, s[4:5]
	v_cmp_ne_u32_e64 s[4:5], 5, v2
	v_cmp_gt_f32_e64 s[6:7], v7, v5
	s_and_b64 s[4:5], s[4:5], s[6:7]
	v_cndmask_b32_e64 v2, v5, v7, s[4:5]
	v_cmp_gt_f32_e32 vcc, v4, v2
	s_and_b64 vcc, s[2:3], vcc
	s_nop 0
	v_cndmask_b32_e32 v2, v2, v4, vcc
	s_and_saveexec_b64 s[2:3], s[0:1]
	s_cbranch_execz .LBB0_12
	v_cmp_gt_f32_e32 vcc, v1, v2
	s_and_saveexec_b64 s[0:1], vcc
	v_mov_b32_e32 v2, v1
	s_or_b64 exec, exec, s[0:1]
	v_mov_b32_e32 v1, v3
